# SGU spatial phase: next unit's SSQ/WSB/b_s/g_v/V^T loads prefetched one unit ahead into spare registers, copied at unit top
# baseline (speedup 1.0000x reference)
.LBB0_1859:
	s_cmp_lt_i32 s92, 25
	s_cselect_b64 s[4:5], -1, 0
	s_cmp_gt_i32 s93, 24
	s_cselect_b64 s[6:7], -1, 0
	s_and_b64 s[4:5], s[4:5], s[6:7]
	s_andn2_b64 vcc, exec, s[4:5]
	s_mov_b32 s4, 24
	s_cbranch_vccnz .LBB0_1921
	s_cmpk_gt_i32 s89, 0xcbf
	s_mov_b32 s6, 22
	s_cbranch_scc1 .LBB0_1871
	s_add_u32 s3, s26, 0x21d00000
	s_addc_u32 s22, s27, 0
	s_add_u32 s23, s26, 0x28500000
	s_addc_u32 s28, s27, 0
	s_add_u32 s29, s26, 0x32d00000
	s_addc_u32 s30, s27, 0
	s_add_u32 s31, s26, 0x500000
	s_addc_u32 s33, s27, 0
	s_ashr_i32 s7, s6, 31
	s_lshl_b64 s[6:7], s[6:7], 3
	s_add_u32 s6, s0, s6
	s_addc_u32 s7, s1, s7
	s_ashr_i32 s5, s4, 31
	s_lshl_b64 s[4:5], s[4:5], 3
	s_add_u32 s4, s0, s4
	s_addc_u32 s5, s1, s5
	s_load_dwordx2 s[8:9], s[6:7], 0x0
	s_load_dwordx2 s[10:11], s[4:5], 0x0
	s_lshl_b32 s4, s88, 5
	s_add_i32 s12, s4, 0
	s_waitcnt vmcnt(0)
	v_ashrrev_i32_e32 v2, 4, v250
	s_add_i32 s6, 0, 0x11000
	s_lshl_b32 s13, s88, 6
	v_lshlrev_b32_e32 v20, 3, v2
	v_and_b32_e32 v3, -16, v250
	s_waitcnt lgkmcnt(0)
	s_add_u32 s8, s8, s13
	v_lshlrev_b32_e32 v2, 2, v2
	v_and_b32_e32 v1, 15, v250
	v_add_u32_e32 v4, 0, v3
	s_addc_u32 s9, s9, 0
	v_ashrrev_i32_e32 v3, 31, v2
	s_movk_i32 s4, 0x80
	v_ashrrev_i32_e32 v171, 31, v170
	v_lshl_add_u32 v26, v170, 2, s6
	s_movk_i32 s6, 0x800
	v_lshl_add_u64 v[22:23], v[2:3], 2, s[8:9]
	v_add_u32_e32 v2, s12, v20
	v_mul_u32_u24_e32 v3, 0x110, v1
	v_cmp_gt_i32_e64 s[4:5], s4, v170
	v_lshl_add_u64 v[18:19], v[170:171], 2, s[96:97]
	v_lshl_or_b32 v27, s88, 4, v1
	v_ashrrev_i32_e32 v21, 31, v20
	v_cmp_gt_i32_e64 s[6:7], s6, v170
	s_movk_i32 s36, 0x110
	v_lshlrev_b32_e32 v28, 3, v170
	v_mov_b32_e32 v29, 0x358637bd
	s_mov_b32 s37, 0xf800000
	v_mov_b32_e32 v30, 0x260
	v_mov_b32_e32 v25, 0
	s_movk_i32 s40, 0x5ff
	v_add_u32_e32 v31, v4, v3
	v_add_u32_e32 v32, v2, v3
	s_movk_i32 s41, 0x1800
	v_and_b32_e32 v197, 0x7f, v170
	v_lshlrev_b32_e32 v197, 2, v197
	s_mov_b32 s101, s89
	s_mul_hi_i32 s48, s101, 0x2aaaaaab
	s_ashr_i32 s48, s48, 2
	v_lshl_add_u32 v196, s48, 9, v197
	global_load_dword v172, v196, s[96:97]
	v_add_u32_e32 v199, 0x11000, v196
	global_load_dword v173, v199, s[96:97]
	v_add_u32_e32 v198, 0x22000, v196
	global_load_dword v174, v198, s[96:97]
	v_add_u32_e32 v199, 0x33000, v196
	global_load_dword v175, v199, s[96:97]
	v_add_u32_e32 v198, 0x44000, v196
	global_load_dword v176, v198, s[96:97]
	v_add_u32_e32 v199, 0x55000, v196
	global_load_dword v177, v199, s[96:97]
	v_add_u32_e32 v198, 0x66000, v196
	global_load_dword v178, v198, s[96:97]
	v_add_u32_e32 v199, 0x77000, v196
	global_load_dword v179, v199, s[96:97]
	v_add_u32_e32 v198, 0x88000, v196
	global_load_dword v180, v198, s[96:97]
	v_add_u32_e32 v199, 0x99000, v196
	global_load_dword v181, v199, s[96:97]
	v_add_u32_e32 v198, 0xaa000, v196
	global_load_dword v182, v198, s[96:97]
	v_add_u32_e32 v199, 0xbb000, v196
	global_load_dword v183, v199, s[96:97]
	v_add_u32_e32 v198, 0xcc000, v196
	global_load_dword v184, v198, s[96:97]
	v_add_u32_e32 v199, 0xdd000, v196
	global_load_dword v185, v199, s[96:97]
	v_add_u32_e32 v198, 0xee000, v196
	global_load_dword v186, v198, s[96:97]
	v_add_u32_e32 v199, 0xff000, v196
	global_load_dword v187, v199, s[96:97]
	v_add_u32_e32 v198, 0x110000, v196
	global_load_dword v188, v198, s[96:97]
	v_add_u32_e32 v199, 0x121000, v196
	global_load_dword v189, v199, s[96:97]
	v_add_u32_e32 v198, 0x132000, v196
	global_load_dword v190, v198, s[96:97]
	v_add_u32_e32 v199, 0x143000, v196
	global_load_dword v191, v199, s[96:97]
	v_add_u32_e32 v198, 0x154000, v196
	global_load_dword v192, v198, s[96:97]
	v_add_u32_e32 v199, 0x165000, v196
	global_load_dword v193, v199, s[96:97]
	v_add_u32_e32 v198, 0x176000, v196
	global_load_dword v194, v198, s[96:97]
	v_add_u32_e32 v199, 0x187000, v196
	global_load_dword v195, v199, s[96:97]
	s_mul_hi_i32 s46, s101, 0x2aaaaaab
	s_lshr_b32 s47, s46, 31
	s_ashr_i32 s48, s46, 2
	s_add_i32 s48, s48, s47
	s_mul_i32 s53, s48, 0xffffffe8
	s_add_i32 s53, s53, s101
	s_mul_hi_i32 s54, s53, 0x55555556
	s_mul_i32 s55, s54, -3
	s_add_i32 s55, s55, s53
	s_lshl_b32 s55, s55, 7
	s_mul_i32 s53, s54, 0x180
	s_add_i32 s55, s55, s53
	v_lshlrev_b32_e32 v244, 4, v170
	v_lshl_add_u32 v244, s54, 15, v244
	v_mov_b32_e32 v247, s33
	v_add_co_u32_e32 v246, vcc, s31, v244
	s_nop 1
	v_addc_co_u32_e32 v247, vcc, 0, v247, vcc
	global_load_dwordx4 v[200:203], v[246:247], off
	v_add_co_u32_e32 v246, vcc, 0x2000, v246
	s_nop 1
	v_addc_co_u32_e32 v247, vcc, 0, v247, vcc
	global_load_dwordx4 v[204:207], v[246:247], off
	v_add_co_u32_e32 v246, vcc, 0x2000, v246
	s_nop 1
	v_addc_co_u32_e32 v247, vcc, 0, v247, vcc
	global_load_dwordx4 v[208:211], v[246:247], off
	v_add_co_u32_e32 v246, vcc, 0x2000, v246
	s_nop 1
	v_addc_co_u32_e32 v247, vcc, 0, v247, vcc
	global_load_dwordx4 v[212:215], v[246:247], off
	v_lshl_or_b32 v245, s54, 7, v1
	v_lshlrev_b32_e32 v245, 2, v245
	global_load_dword v216, v245, s[10:11]
	global_load_dword v217, v245, s[10:11] offset:64
	global_load_dword v218, v245, s[10:11] offset:128
	global_load_dword v219, v245, s[10:11] offset:192
	global_load_dword v220, v245, s[10:11] offset:256
	global_load_dword v221, v245, s[10:11] offset:320
	global_load_dword v222, v245, s[10:11] offset:384
	global_load_dword v223, v245, s[10:11] offset:448
	v_mov_b32_e32 v248, s55
	v_mov_b32_e32 v249, 0
	v_lshl_add_u64 v[248:249], v[248:249], 2, v[22:23]
	global_load_dwordx4 v[224:227], v[248:249], off
	s_mul_i32 s46, s48, 0xffffffe8
	s_add_i32 s46, s46, s101
	s_mul_hi_i32 s47, s46, 0x55555556
	s_lshr_b32 s51, s47, 31
	s_add_i32 s52, s47, s51
	s_mul_i32 s47, s52, -3
	s_add_i32 s47, s47, s46
	s_mul_i32 s46, s52, 0x180
	s_lshl_b32 s47, s47, 7
	s_add_i32 s46, s47, s46
	s_mul_hi_i32 s47, s48, 0xc0000
	s_mul_i32 s48, s48, 0xc0000
	v_add_u32_e32 v252, s46, v27
	s_add_u32 s48, s23, s48
	v_ashrrev_i32_e32 v253, 31, v252
	s_addc_u32 s49, s28, s47
	v_lshlrev_b64 v[252:253], 8, v[252:253]
	v_lshl_add_u64 v[252:253], s[48:49], 0, v[252:253]
	v_lshl_add_u64 v[252:253], v[20:21], 1, v[252:253]
	global_load_dwordx4 v[240:243], v[252:253], off
	global_load_dwordx4 v[236:239], v[252:253], off offset:64
	global_load_dwordx4 v[232:235], v[252:253], off offset:128
	s_nop 0
	global_load_dwordx4 v[228:231], v[252:253], off offset:192
	s_waitcnt vmcnt(0)
	s_mov_b32 s42, s89
	s_branch .LBB0_1863

.LBB0_1863:
	s_mul_hi_i32 s8, s42, 0x2aaaaaab
	s_lshr_b32 s9, s8, 31
	s_ashr_i32 s16, s8, 2
	s_add_i32 s16, s16, s9
	s_lshl_b32 s12, s16, 7
	s_barrier
	s_mul_i32 s98, s16, 0xffffffe8
	s_add_i32 s98, s98, s42
	s_mul_hi_i32 s99, s98, 0x55555556
	s_mul_i32 s100, s99, -3
	s_add_i32 s100, s100, s98
	s_lshl_b32 s100, s100, 7
	s_mul_i32 s98, s99, 0x180
	s_add_i32 s100, s100, s98
	s_waitcnt vmcnt(4)
	v_mov_b64_e32 v[138:139], v[200:201]
	v_mov_b64_e32 v[140:141], v[202:203]
	v_mov_b64_e32 v[142:143], v[204:205]
	v_mov_b64_e32 v[144:145], v[206:207]
	v_mov_b64_e32 v[146:147], v[208:209]
	v_mov_b64_e32 v[148:149], v[210:211]
	v_mov_b64_e32 v[150:151], v[212:213]
	v_mov_b64_e32 v[152:153], v[214:215]
	v_mov_b64_e32 v[104:105], v[216:217]
	v_mov_b64_e32 v[106:107], v[218:219]
	v_mov_b64_e32 v[108:109], v[220:221]
	v_mov_b64_e32 v[110:111], v[222:223]
	v_mov_b64_e32 v[116:117], v[224:225]
	v_mov_b64_e32 v[118:119], v[226:227]
	s_and_saveexec_b64 s[14:15], s[4:5]
	s_cbranch_execz .LBB0_1865
	s_waitcnt vmcnt(36)
	v_add_f32_e32 v3, 0, v172
	s_waitcnt vmcnt(35)
	v_add_f32_e32 v3, v3, v173
	s_waitcnt vmcnt(34)
	v_add_f32_e32 v3, v3, v174
	s_waitcnt vmcnt(33)
	v_add_f32_e32 v3, v3, v175
	s_waitcnt vmcnt(32)
	v_add_f32_e32 v3, v3, v176
	s_waitcnt vmcnt(31)
	v_add_f32_e32 v3, v3, v177
	s_waitcnt vmcnt(30)
	v_add_f32_e32 v3, v3, v178
	s_waitcnt vmcnt(29)
	v_add_f32_e32 v3, v3, v179
	s_waitcnt vmcnt(28)
	v_add_f32_e32 v3, v3, v180
	s_waitcnt vmcnt(27)
	v_add_f32_e32 v3, v3, v181
	s_waitcnt vmcnt(26)
	v_add_f32_e32 v3, v3, v182
	s_waitcnt vmcnt(25)
	v_add_f32_e32 v3, v3, v183
	s_waitcnt vmcnt(24)
	v_add_f32_e32 v3, v3, v184
	s_waitcnt vmcnt(23)
	v_add_f32_e32 v3, v3, v185
	s_waitcnt vmcnt(22)
	v_add_f32_e32 v3, v3, v186
	s_waitcnt vmcnt(21)
	v_add_f32_e32 v3, v3, v187
	s_waitcnt vmcnt(20)
	v_add_f32_e32 v3, v3, v188
	s_waitcnt vmcnt(19)
	v_add_f32_e32 v3, v3, v189
	s_waitcnt vmcnt(18)
	v_add_f32_e32 v3, v3, v190
	s_waitcnt vmcnt(17)
	v_add_f32_e32 v3, v3, v191
	s_waitcnt vmcnt(16)
	v_add_f32_e32 v3, v3, v192
	s_waitcnt vmcnt(15)
	v_add_f32_e32 v3, v3, v193
	s_waitcnt vmcnt(14)
	v_add_f32_e32 v3, v3, v194
	s_waitcnt vmcnt(13)
	v_add_f32_e32 v2, v3, v195
	v_fmamk_f32 v2, v2, 0x39aaaaab, v29
	v_mul_f32_e32 v3, 0x4f800000, v2
	v_cmp_gt_f32_e32 vcc, s37, v2
	s_nop 1
	v_cndmask_b32_e32 v2, v2, v3, vcc
	v_sqrt_f32_e32 v3, v2
	s_nop 0
	v_add_u32_e32 v4, -1, v3
	v_fma_f32 v5, -v4, v3, v2
	v_cmp_ge_f32_e64 s[8:9], 0, v5
	v_add_u32_e32 v5, 1, v3
	s_nop 0
	v_cndmask_b32_e64 v4, v3, v4, s[8:9]
	v_fma_f32 v3, -v5, v3, v2
	v_cmp_lt_f32_e64 s[8:9], 0, v3
	s_nop 1
	v_cndmask_b32_e64 v3, v4, v5, s[8:9]
	v_mul_f32_e32 v4, 0x37800000, v3
	v_cndmask_b32_e32 v3, v3, v4, vcc
	v_cmp_class_f32_e32 vcc, v2, v30
	s_nop 1
	v_cndmask_b32_e32 v2, v3, v2, vcc
	v_div_scale_f32 v3, s[8:9], v2, v2, 1.0
	v_rcp_f32_e32 v4, v3
	s_nop 0
	v_fma_f32 v5, -v3, v4, 1.0
	v_fmac_f32_e32 v4, v5, v4
	v_div_scale_f32 v5, vcc, 1.0, v2, 1.0
	v_mul_f32_e32 v6, v5, v4
	v_fma_f32 v7, -v3, v6, v5
	v_fmac_f32_e32 v6, v7, v4
	v_fma_f32 v3, -v3, v6, v5
	v_div_fmas_f32 v3, v3, v4, v6
	v_div_fixup_f32 v2, v3, v2, 1.0
	ds_write_b32 v26, v2
.LBB0_1865:
	s_or_b64 exec, exec, s[14:15]
	s_mul_i32 s8, s16, 0xffffffe8
	s_add_i32 s8, s8, s42
	s_mul_hi_i32 s9, s8, 0x55555556
	s_lshr_b32 s13, s9, 31
	s_add_i32 s14, s9, s13
	s_mul_i32 s9, s14, -3
	s_add_i32 s9, s9, s8
	s_mul_i32 s8, s14, 0x180
	s_lshl_b32 s9, s9, 7
	s_add_i32 s8, s9, s8
	s_mul_hi_i32 s9, s16, 0xc0000
	s_mul_i32 s16, s16, 0xc0000
	s_add_u32 s16, s23, s16
	s_addc_u32 s17, s28, s9
	v_mov_b64_e32 v[2:3], v[228:229]
	v_mov_b64_e32 v[4:5], v[230:231]
	v_mov_b64_e32 v[6:7], v[232:233]
	v_mov_b64_e32 v[8:9], v[234:235]
	v_mov_b64_e32 v[10:11], v[236:237]
	v_mov_b64_e32 v[12:13], v[238:239]
	v_mov_b64_e32 v[14:15], v[240:241]
	v_mov_b64_e32 v[16:17], v[242:243]
	v_lshrrev_b32_e32 v164, 4, v170
	v_add_u32_e32 v164, s12, v164
	v_and_b32_e32 v165, 15, v170
	v_lshlrev_b32_e32 v165, 4, v165
	v_lshl_add_u32 v165, s8, 1, v165
	v_mov_b32_e32 v136, s3
	v_mov_b32_e32 v137, s22
	v_mad_u64_u32 v[136:137], s[20:21], v164, s41, v[136:137]
	v_add_co_u32_e32 v136, vcc, v136, v165
	s_nop 1
	v_addc_co_u32_e32 v137, vcc, 0, v137, vcc
	global_load_dwordx4 v[120:123], v[136:137], off
	v_add_co_u32_e32 v136, vcc, 0x30000, v136
	s_nop 1
	v_addc_co_u32_e32 v137, vcc, 0, v137, vcc
	global_load_dwordx4 v[124:127], v[136:137], off
	v_add_co_u32_e32 v136, vcc, 0x30000, v136
	s_nop 1
	v_addc_co_u32_e32 v137, vcc, 0, v137, vcc
	global_load_dwordx4 v[128:131], v[136:137], off
	v_add_co_u32_e32 v136, vcc, 0x30000, v136
	s_nop 1
	v_addc_co_u32_e32 v137, vcc, 0, v137, vcc
	global_load_dwordx4 v[132:135], v[136:137], off
	s_waitcnt lgkmcnt(0)
	s_barrier
	v_and_b32_e32 v166, 15, v170
	v_lshlrev_b32_e32 v166, 5, v166
	v_add_u32_e32 v166, 0x11000, v166
	ds_read_b128 v[156:159], v166
	ds_read_b128 v[160:163], v166 offset:16
	v_lshrrev_b32_e32 v167, 4, v170
	v_mul_u32_u24_e32 v167, 0x110, v167
	v_and_b32_e32 v166, 15, v170
	v_lshl_add_u32 v167, v166, 4, v167
	s_waitcnt vmcnt(17) lgkmcnt(0)
	v_lshlrev_b32_e32 v168, 16, v138
	v_and_b32_e32 v138, 0xffff0000, v138
	v_mul_f32_e32 v168, v156, v168
	v_mul_f32_e32 v138, v157, v138
	v_cvt_pk_bf16_f32 v138, v168, v138
	v_lshlrev_b32_e32 v168, 16, v139
	v_and_b32_e32 v139, 0xffff0000, v139
	v_mul_f32_e32 v168, v158, v168
	v_mul_f32_e32 v139, v159, v139
	v_cvt_pk_bf16_f32 v139, v168, v139
	v_lshlrev_b32_e32 v168, 16, v140
	v_and_b32_e32 v140, 0xffff0000, v140
	v_mul_f32_e32 v168, v160, v168
	v_mul_f32_e32 v140, v161, v140
	v_cvt_pk_bf16_f32 v140, v168, v140
	v_lshlrev_b32_e32 v168, 16, v141
	v_and_b32_e32 v141, 0xffff0000, v141
	v_mul_f32_e32 v168, v162, v168
	v_mul_f32_e32 v141, v163, v141
	v_cvt_pk_bf16_f32 v141, v168, v141
	ds_write_b128 v167, v[138:141]
	v_lshlrev_b32_e32 v168, 16, v142
	v_and_b32_e32 v142, 0xffff0000, v142
	v_mul_f32_e32 v168, v156, v168
	v_mul_f32_e32 v142, v157, v142
	v_cvt_pk_bf16_f32 v142, v168, v142
	v_lshlrev_b32_e32 v168, 16, v143
	v_and_b32_e32 v143, 0xffff0000, v143
	v_mul_f32_e32 v168, v158, v168
	v_mul_f32_e32 v143, v159, v143
	v_cvt_pk_bf16_f32 v143, v168, v143
	v_lshlrev_b32_e32 v168, 16, v144
	v_and_b32_e32 v144, 0xffff0000, v144
	v_mul_f32_e32 v168, v160, v168
	v_mul_f32_e32 v144, v161, v144
	v_cvt_pk_bf16_f32 v144, v168, v144
	v_lshlrev_b32_e32 v168, 16, v145
	v_and_b32_e32 v145, 0xffff0000, v145
	v_mul_f32_e32 v168, v162, v168
	v_mul_f32_e32 v145, v163, v145
	v_cvt_pk_bf16_f32 v145, v168, v145
	ds_write_b128 v167, v[142:145] offset:8704
	v_lshlrev_b32_e32 v168, 16, v146
	v_and_b32_e32 v146, 0xffff0000, v146
	v_mul_f32_e32 v168, v156, v168
	v_mul_f32_e32 v146, v157, v146
	v_cvt_pk_bf16_f32 v146, v168, v146
	v_lshlrev_b32_e32 v168, 16, v147
	v_and_b32_e32 v147, 0xffff0000, v147
	v_mul_f32_e32 v168, v158, v168
	v_mul_f32_e32 v147, v159, v147
	v_cvt_pk_bf16_f32 v147, v168, v147
	v_lshlrev_b32_e32 v168, 16, v148
	v_and_b32_e32 v148, 0xffff0000, v148
	v_mul_f32_e32 v168, v160, v168
	v_mul_f32_e32 v148, v161, v148
	v_cvt_pk_bf16_f32 v148, v168, v148
	v_lshlrev_b32_e32 v168, 16, v149
	v_and_b32_e32 v149, 0xffff0000, v149
	v_mul_f32_e32 v168, v162, v168
	v_mul_f32_e32 v149, v163, v149
	v_cvt_pk_bf16_f32 v149, v168, v149
	ds_write_b128 v167, v[146:149] offset:17408
	v_lshlrev_b32_e32 v168, 16, v150
	v_and_b32_e32 v150, 0xffff0000, v150
	v_mul_f32_e32 v168, v156, v168
	v_mul_f32_e32 v150, v157, v150
	v_cvt_pk_bf16_f32 v150, v168, v150
	v_lshlrev_b32_e32 v168, 16, v151
	v_and_b32_e32 v151, 0xffff0000, v151
	v_mul_f32_e32 v168, v158, v168
	v_mul_f32_e32 v151, v159, v151
	v_cvt_pk_bf16_f32 v151, v168, v151
	v_lshlrev_b32_e32 v168, 16, v152
	v_and_b32_e32 v152, 0xffff0000, v152
	v_mul_f32_e32 v168, v160, v168
	v_mul_f32_e32 v152, v161, v152
	v_cvt_pk_bf16_f32 v152, v168, v152
	v_lshlrev_b32_e32 v168, 16, v153
	v_and_b32_e32 v153, 0xffff0000, v153
	v_mul_f32_e32 v168, v162, v168
	v_mul_f32_e32 v153, v163, v153
	v_cvt_pk_bf16_f32 v153, v168, v153
	ds_write_b128 v167, v[150:153] offset:26112
	s_waitcnt lgkmcnt(0)
	s_barrier
	ds_read_b128 v[34:37], v31
	ds_read_b128 v[38:41], v31 offset:64
	ds_read_b128 v[42:45], v31 offset:4352
	ds_read_b128 v[46:49], v31 offset:4416
	ds_read_b128 v[50:53], v31 offset:8704
	ds_read_b128 v[54:57], v31 offset:8768
	ds_read_b128 v[58:61], v31 offset:13056
	ds_read_b128 v[62:65], v31 offset:13120
	s_add_i32 s101, s42, s34
	s_min_i32 s101, s101, 0xcbf
	s_mul_hi_i32 s48, s101, 0x2aaaaaab
	s_ashr_i32 s48, s48, 2
	v_lshl_add_u32 v196, s48, 9, v197
	global_load_dword v172, v196, s[96:97]
	v_add_u32_e32 v199, 0x11000, v196
	global_load_dword v173, v199, s[96:97]
	v_add_u32_e32 v198, 0x22000, v196
	global_load_dword v174, v198, s[96:97]
	v_add_u32_e32 v199, 0x33000, v196
	global_load_dword v175, v199, s[96:97]
	v_add_u32_e32 v198, 0x44000, v196
	global_load_dword v176, v198, s[96:97]
	v_add_u32_e32 v199, 0x55000, v196
	global_load_dword v177, v199, s[96:97]
	v_add_u32_e32 v198, 0x66000, v196
	global_load_dword v178, v198, s[96:97]
	v_add_u32_e32 v199, 0x77000, v196
	global_load_dword v179, v199, s[96:97]
	v_add_u32_e32 v198, 0x88000, v196
	global_load_dword v180, v198, s[96:97]
	v_add_u32_e32 v199, 0x99000, v196
	global_load_dword v181, v199, s[96:97]
	v_add_u32_e32 v198, 0xaa000, v196
	global_load_dword v182, v198, s[96:97]
	v_add_u32_e32 v199, 0xbb000, v196
	global_load_dword v183, v199, s[96:97]
	v_add_u32_e32 v198, 0xcc000, v196
	global_load_dword v184, v198, s[96:97]
	v_add_u32_e32 v199, 0xdd000, v196
	global_load_dword v185, v199, s[96:97]
	v_add_u32_e32 v198, 0xee000, v196
	global_load_dword v186, v198, s[96:97]
	v_add_u32_e32 v199, 0xff000, v196
	global_load_dword v187, v199, s[96:97]
	v_add_u32_e32 v198, 0x110000, v196
	global_load_dword v188, v198, s[96:97]
	v_add_u32_e32 v199, 0x121000, v196
	global_load_dword v189, v199, s[96:97]
	v_add_u32_e32 v198, 0x132000, v196
	global_load_dword v190, v198, s[96:97]
	v_add_u32_e32 v199, 0x143000, v196
	global_load_dword v191, v199, s[96:97]
	v_add_u32_e32 v198, 0x154000, v196
	global_load_dword v192, v198, s[96:97]
	v_add_u32_e32 v199, 0x165000, v196
	global_load_dword v193, v199, s[96:97]
	v_add_u32_e32 v198, 0x176000, v196
	global_load_dword v194, v198, s[96:97]
	v_add_u32_e32 v199, 0x187000, v196
	global_load_dword v195, v199, s[96:97]
	s_mul_hi_i32 s46, s101, 0x2aaaaaab
	s_lshr_b32 s47, s46, 31
	s_ashr_i32 s48, s46, 2
	s_add_i32 s48, s48, s47
	s_mul_i32 s53, s48, 0xffffffe8
	s_add_i32 s53, s53, s101
	s_mul_hi_i32 s54, s53, 0x55555556
	s_mul_i32 s55, s54, -3
	s_add_i32 s55, s55, s53
	s_lshl_b32 s55, s55, 7
	s_mul_i32 s53, s54, 0x180
	s_add_i32 s55, s55, s53
	v_lshlrev_b32_e32 v244, 4, v170
	v_lshl_add_u32 v244, s54, 15, v244
	v_mov_b32_e32 v247, s33
	v_add_co_u32_e32 v246, vcc, s31, v244
	s_nop 1
	v_addc_co_u32_e32 v247, vcc, 0, v247, vcc
	global_load_dwordx4 v[200:203], v[246:247], off
	v_add_co_u32_e32 v246, vcc, 0x2000, v246
	s_nop 1
	v_addc_co_u32_e32 v247, vcc, 0, v247, vcc
	global_load_dwordx4 v[204:207], v[246:247], off
	v_add_co_u32_e32 v246, vcc, 0x2000, v246
	s_nop 1
	v_addc_co_u32_e32 v247, vcc, 0, v247, vcc
	global_load_dwordx4 v[208:211], v[246:247], off
	v_add_co_u32_e32 v246, vcc, 0x2000, v246
	s_nop 1
	v_addc_co_u32_e32 v247, vcc, 0, v247, vcc
	global_load_dwordx4 v[212:215], v[246:247], off
	v_lshl_or_b32 v245, s54, 7, v1
	v_lshlrev_b32_e32 v245, 2, v245
	global_load_dword v216, v245, s[10:11]
	global_load_dword v217, v245, s[10:11] offset:64
	global_load_dword v218, v245, s[10:11] offset:128
	global_load_dword v219, v245, s[10:11] offset:192
	global_load_dword v220, v245, s[10:11] offset:256
	global_load_dword v221, v245, s[10:11] offset:320
	global_load_dword v222, v245, s[10:11] offset:384
	global_load_dword v223, v245, s[10:11] offset:448
	v_mov_b32_e32 v248, s55
	v_mov_b32_e32 v249, 0
	v_lshl_add_u64 v[248:249], v[248:249], 2, v[22:23]
	global_load_dwordx4 v[224:227], v[248:249], off
	s_mul_i32 s46, s48, 0xffffffe8
	s_add_i32 s46, s46, s101
	s_mul_hi_i32 s47, s46, 0x55555556
	s_lshr_b32 s51, s47, 31
	s_add_i32 s52, s47, s51
	s_mul_i32 s47, s52, -3
	s_add_i32 s47, s47, s46
	s_mul_i32 s46, s52, 0x180
	s_lshl_b32 s47, s47, 7
	s_add_i32 s46, s47, s46
	s_mul_hi_i32 s47, s48, 0xc0000
	s_mul_i32 s48, s48, 0xc0000
	v_add_u32_e32 v252, s46, v27
	s_add_u32 s48, s23, s48
	v_ashrrev_i32_e32 v253, 31, v252
	s_addc_u32 s49, s28, s47
	v_lshlrev_b64 v[252:253], 8, v[252:253]
	v_lshl_add_u64 v[252:253], s[48:49], 0, v[252:253]
	v_lshl_add_u64 v[252:253], v[20:21], 1, v[252:253]
	global_load_dwordx4 v[240:243], v[252:253], off
	global_load_dwordx4 v[236:239], v[252:253], off offset:64
	global_load_dwordx4 v[232:235], v[252:253], off offset:128
	s_nop 0
	global_load_dwordx4 v[228:231], v[252:253], off offset:192
	s_waitcnt vmcnt(48) lgkmcnt(7)
	v_mfma_f32_16x16x32_bf16 v[34:37], v[14:17], v[34:37], 0
	s_ashr_i32 s9, s8, 31
	ds_read_b128 v[66:69], v31 offset:17408
	ds_read_b128 v[70:73], v31 offset:17472
	ds_read_b128 v[74:77], v31 offset:21760
	ds_read_b128 v[78:81], v31 offset:21824
	s_waitcnt lgkmcnt(9)
	v_mfma_f32_16x16x32_bf16 v[42:45], v[14:17], v[42:45], 0
	ds_read_b128 v[82:85], v31 offset:26112
	ds_read_b128 v[86:89], v31 offset:26176
	ds_read_b128 v[90:93], v31 offset:30464
	ds_read_b128 v[94:97], v31 offset:30528
	s_waitcnt lgkmcnt(9)
	v_mfma_f32_16x16x32_bf16 v[58:61], v[14:17], v[58:61], 0
	v_mfma_f32_16x16x32_bf16 v[50:53], v[14:17], v[50:53], 0
	s_waitcnt vmcnt(47)
	v_mfma_f32_16x16x32_bf16 v[34:37], v[10:13], v[38:41], v[34:37]
	v_mfma_f32_16x16x32_bf16 v[38:41], v[10:13], v[46:49], v[42:45]
	s_waitcnt lgkmcnt(8)
	v_mfma_f32_16x16x32_bf16 v[46:49], v[10:13], v[62:65], v[58:61]
	s_nop 0
	s_nop 0
	s_nop 0
	v_mfma_f32_16x16x32_bf16 v[42:45], v[10:13], v[54:57], v[50:53]
	s_nop 0
	s_nop 0
	s_nop 0
	s_nop 0
	s_waitcnt lgkmcnt(7)
	v_mfma_f32_16x16x32_bf16 v[66:69], v[14:17], v[66:69], 0
	s_waitcnt lgkmcnt(5)
	v_mfma_f32_16x16x32_bf16 v[74:77], v[14:17], v[74:77], 0
	s_waitcnt lgkmcnt(3)
	v_mfma_f32_16x16x32_bf16 v[82:85], v[14:17], v[82:85], 0
	s_waitcnt lgkmcnt(1)
	v_mfma_f32_16x16x32_bf16 v[14:17], v[14:17], v[90:93], 0
	v_mfma_f32_16x16x32_bf16 v[50:53], v[10:13], v[70:73], v[66:69]
	v_mfma_f32_16x16x32_bf16 v[58:61], v[10:13], v[78:81], v[74:77]
	v_mfma_f32_16x16x32_bf16 v[62:65], v[10:13], v[86:89], v[82:85]
	s_waitcnt lgkmcnt(0)
	v_mfma_f32_16x16x32_bf16 v[10:13], v[10:13], v[94:97], v[14:17]
	s_nop 2
	ds_read_b128 v[14:17], v31 offset:128
	ds_read_b128 v[66:69], v31 offset:192
	s_waitcnt vmcnt(46) lgkmcnt(1)
	v_mfma_f32_16x16x32_bf16 v[14:17], v[6:9], v[14:17], v[34:37]
	s_nop 2
	ds_read_b128 v[34:37], v31 offset:4480
	ds_read_b128 v[70:73], v31 offset:4544
	s_waitcnt lgkmcnt(1)
	v_mfma_f32_16x16x32_bf16 v[34:37], v[6:9], v[34:37], v[38:41]
	s_nop 2
	ds_read_b128 v[38:41], v31 offset:8832
	ds_read_b128 v[74:77], v31 offset:8896
	s_waitcnt lgkmcnt(1)
	v_mfma_f32_16x16x32_bf16 v[38:41], v[6:9], v[38:41], v[42:45]
	s_nop 2
	ds_read_b128 v[42:45], v31 offset:13184
	ds_read_b128 v[78:81], v31 offset:13248
	s_waitcnt lgkmcnt(1)
	v_mfma_f32_16x16x32_bf16 v[42:45], v[6:9], v[42:45], v[46:49]
	s_nop 2
	ds_read_b128 v[46:49], v31 offset:17536
	ds_read_b128 v[82:85], v31 offset:17600
	s_waitcnt vmcnt(45)
	v_mfma_f32_16x16x32_bf16 v[14:17], v[2:5], v[66:69], v[14:17]
	s_waitcnt lgkmcnt(1)
	v_mfma_f32_16x16x32_bf16 v[46:49], v[6:9], v[46:49], v[50:53]
	s_nop 2
	ds_read_b128 v[50:53], v31 offset:21888
	ds_read_b128 v[86:89], v31 offset:21952
	s_waitcnt vmcnt(45)
	v_fma_f32 v14, v14, v116, v104
	v_fma_f32 v15, v15, v117, v104
	s_waitcnt lgkmcnt(1)
	v_mfma_f32_16x16x32_bf16 v[50:53], v[6:9], v[50:53], v[58:61]
	s_nop 2
	ds_read_b128 v[58:61], v31 offset:26240
	ds_read_b128 v[90:93], v31 offset:26304
	ds_read_b128 v[94:97], v31 offset:30592
	ds_read_b128 v[98:101], v31 offset:30656
	v_cvt_pk_bf16_f32 v14, v14, v15
	v_fma_f32 v15, v16, v118, v104
	v_fmac_f32_e32 v104, v17, v119
	v_cvt_pk_bf16_f32 v15, v15, v104
	s_nop 0
	s_waitcnt lgkmcnt(3)
	v_mfma_f32_16x16x32_bf16 v[58:61], v[6:9], v[58:61], v[62:65]
	ds_write_b64 v32, v[14:15] offset:34816
	s_waitcnt lgkmcnt(2)
	v_mfma_f32_16x16x32_bf16 v[6:9], v[6:9], v[94:97], v[10:13]
	v_mfma_f32_16x16x32_bf16 v[10:13], v[2:5], v[70:73], v[34:37]
	s_waitcnt vmcnt(45)
	s_nop 6
	v_fma_f32 v10, v10, v116, v105
	v_fma_f32 v11, v11, v117, v105
	v_fma_f32 v12, v12, v118, v105
	v_fmac_f32_e32 v105, v13, v119
	v_cvt_pk_bf16_f32 v14, v10, v11
	v_cvt_pk_bf16_f32 v15, v12, v105
	s_nop 0
	v_mfma_f32_16x16x32_bf16 v[10:13], v[2:5], v[74:77], v[38:41]
	ds_write_b64 v32, v[14:15] offset:39168
	s_waitcnt vmcnt(45)
	s_nop 5
	v_fma_f32 v10, v10, v116, v106
	v_fma_f32 v11, v11, v117, v106
	v_fma_f32 v12, v12, v118, v106
	v_fmac_f32_e32 v106, v13, v119
	v_cvt_pk_bf16_f32 v14, v10, v11
	v_cvt_pk_bf16_f32 v15, v12, v106
	s_nop 0
	v_mfma_f32_16x16x32_bf16 v[10:13], v[2:5], v[78:81], v[42:45]
	ds_write_b64 v32, v[14:15] offset:43520
	s_waitcnt vmcnt(45)
	s_nop 5
	v_fma_f32 v10, v10, v116, v107
	v_fma_f32 v11, v11, v117, v107
	v_fma_f32 v12, v12, v118, v107
	v_fmac_f32_e32 v107, v13, v119
	v_cvt_pk_bf16_f32 v14, v10, v11
	v_cvt_pk_bf16_f32 v15, v12, v107
	s_nop 0
	v_mfma_f32_16x16x32_bf16 v[10:13], v[2:5], v[82:85], v[46:49]
	ds_write_b64 v32, v[14:15] offset:47872
	s_waitcnt vmcnt(45)
	s_nop 5
	v_fma_f32 v10, v10, v116, v108
	v_fma_f32 v11, v11, v117, v108
	v_fma_f32 v12, v12, v118, v108
	v_fmac_f32_e32 v108, v13, v119
	v_cvt_pk_bf16_f32 v14, v10, v11
	v_cvt_pk_bf16_f32 v15, v12, v108
	s_nop 0
	v_mfma_f32_16x16x32_bf16 v[10:13], v[2:5], v[86:89], v[50:53]
	ds_write_b64 v32, v[14:15] offset:52224
	s_waitcnt vmcnt(45)
	s_nop 5
	v_fma_f32 v10, v10, v116, v109
	v_fma_f32 v11, v11, v117, v109
	v_fma_f32 v12, v12, v118, v109
	v_fmac_f32_e32 v109, v13, v119
	v_cvt_pk_bf16_f32 v14, v10, v11
	v_cvt_pk_bf16_f32 v15, v12, v109
	s_nop 0
	v_mfma_f32_16x16x32_bf16 v[10:13], v[2:5], v[90:93], v[58:61]
	ds_write_b64 v32, v[14:15] offset:56576
	s_waitcnt lgkmcnt(6)
	v_mfma_f32_16x16x32_bf16 v[2:5], v[2:5], v[98:101], v[6:9]
	s_waitcnt vmcnt(45)
	s_nop 3
	v_fma_f32 v10, v10, v116, v110
	v_fma_f32 v11, v11, v117, v110
	v_fma_f32 v12, v12, v118, v110
	v_fmac_f32_e32 v110, v13, v119
	v_cvt_pk_bf16_f32 v10, v10, v11
	v_cvt_pk_bf16_f32 v11, v12, v110
	s_nop 0
	ds_write_b64 v32, v[10:11] offset:60928
	s_waitcnt vmcnt(45)
	v_fma_f32 v2, v2, v116, v111
	v_fma_f32 v3, v3, v117, v111
	v_fma_f32 v4, v4, v118, v111
	v_fmac_f32_e32 v111, v5, v119
	v_cvt_pk_bf16_f32 v2, v2, v3
	v_cvt_pk_bf16_f32 v3, v4, v111
	ds_write_b64 v32, v[2:3] offset:65280
	s_waitcnt lgkmcnt(0)
	s_barrier
	v_lshrrev_b32_e32 v167, 4, v170
	v_mul_u32_u24_e32 v167, 0x110, v167
	v_and_b32_e32 v166, 15, v170
	v_lshl_add_u32 v167, v166, 4, v167
	v_mov_b32_e32 v136, s29
	v_mov_b32_e32 v137, s30
	v_mad_u64_u32 v[136:137], s[20:21], v164, s41, v[136:137]
	v_add_co_u32_e32 v136, vcc, v136, v165
	s_nop 1
	v_addc_co_u32_e32 v137, vcc, 0, v137, vcc
	ds_read_b128 v[138:141], v167 offset:34816
	ds_read_b128 v[142:145], v167 offset:43520
	ds_read_b128 v[146:149], v167 offset:52224
	ds_read_b128 v[150:153], v167 offset:60928
	s_waitcnt vmcnt(44) lgkmcnt(3)
	v_lshlrev_b32_e32 v168, 16, v138
	v_and_b32_e32 v138, 0xffff0000, v138
	v_lshlrev_b32_e32 v169, 16, v120
	v_and_b32_e32 v120, 0xffff0000, v120
	v_mul_f32_e32 v168, v168, v169
	v_mul_f32_e32 v138, v138, v120
	v_cvt_pk_bf16_f32 v138, v168, v138
	v_lshlrev_b32_e32 v168, 16, v139
	v_and_b32_e32 v139, 0xffff0000, v139
	v_lshlrev_b32_e32 v169, 16, v121
	v_and_b32_e32 v121, 0xffff0000, v121
	v_mul_f32_e32 v168, v168, v169
	v_mul_f32_e32 v139, v139, v121
	v_cvt_pk_bf16_f32 v139, v168, v139
	v_lshlrev_b32_e32 v168, 16, v140
	v_and_b32_e32 v140, 0xffff0000, v140
	v_lshlrev_b32_e32 v169, 16, v122
	v_and_b32_e32 v122, 0xffff0000, v122
	v_mul_f32_e32 v168, v168, v169
	v_mul_f32_e32 v140, v140, v122
	v_cvt_pk_bf16_f32 v140, v168, v140
	v_lshlrev_b32_e32 v168, 16, v141
	v_and_b32_e32 v141, 0xffff0000, v141
	v_lshlrev_b32_e32 v169, 16, v123
	v_and_b32_e32 v123, 0xffff0000, v123
	v_mul_f32_e32 v168, v168, v169
	v_mul_f32_e32 v141, v141, v123
	v_cvt_pk_bf16_f32 v141, v168, v141
	global_store_dwordx4 v[136:137], v[138:141], off
	v_add_co_u32_e32 v136, vcc, 0x30000, v136
	s_nop 1
	v_addc_co_u32_e32 v137, vcc, 0, v137, vcc
	s_waitcnt vmcnt(44) lgkmcnt(2)
	v_lshlrev_b32_e32 v168, 16, v142
	v_and_b32_e32 v142, 0xffff0000, v142
	v_lshlrev_b32_e32 v169, 16, v124
	v_and_b32_e32 v124, 0xffff0000, v124
	v_mul_f32_e32 v168, v168, v169
	v_mul_f32_e32 v142, v142, v124
	v_cvt_pk_bf16_f32 v142, v168, v142
	v_lshlrev_b32_e32 v168, 16, v143
	v_and_b32_e32 v143, 0xffff0000, v143
	v_lshlrev_b32_e32 v169, 16, v125
	v_and_b32_e32 v125, 0xffff0000, v125
	v_mul_f32_e32 v168, v168, v169
	v_mul_f32_e32 v143, v143, v125
	v_cvt_pk_bf16_f32 v143, v168, v143
	v_lshlrev_b32_e32 v168, 16, v144
	v_and_b32_e32 v144, 0xffff0000, v144
	v_lshlrev_b32_e32 v169, 16, v126
	v_and_b32_e32 v126, 0xffff0000, v126
	v_mul_f32_e32 v168, v168, v169
	v_mul_f32_e32 v144, v144, v126
	v_cvt_pk_bf16_f32 v144, v168, v144
	v_lshlrev_b32_e32 v168, 16, v145
	v_and_b32_e32 v145, 0xffff0000, v145
	v_lshlrev_b32_e32 v169, 16, v127
	v_and_b32_e32 v127, 0xffff0000, v127
	v_mul_f32_e32 v168, v168, v169
	v_mul_f32_e32 v145, v145, v127
	v_cvt_pk_bf16_f32 v145, v168, v145
	global_store_dwordx4 v[136:137], v[142:145], off
	v_add_co_u32_e32 v136, vcc, 0x30000, v136
	s_nop 1
	v_addc_co_u32_e32 v137, vcc, 0, v137, vcc
	s_waitcnt vmcnt(44) lgkmcnt(1)
	v_lshlrev_b32_e32 v168, 16, v146
	v_and_b32_e32 v146, 0xffff0000, v146
	v_lshlrev_b32_e32 v169, 16, v128
	v_and_b32_e32 v128, 0xffff0000, v128
	v_mul_f32_e32 v168, v168, v169
	v_mul_f32_e32 v146, v146, v128
	v_cvt_pk_bf16_f32 v146, v168, v146
	v_lshlrev_b32_e32 v168, 16, v147
	v_and_b32_e32 v147, 0xffff0000, v147
	v_lshlrev_b32_e32 v169, 16, v129
	v_and_b32_e32 v129, 0xffff0000, v129
	v_mul_f32_e32 v168, v168, v169
	v_mul_f32_e32 v147, v147, v129
	v_cvt_pk_bf16_f32 v147, v168, v147
	v_lshlrev_b32_e32 v168, 16, v148
	v_and_b32_e32 v148, 0xffff0000, v148
	v_lshlrev_b32_e32 v169, 16, v130
	v_and_b32_e32 v130, 0xffff0000, v130
	v_mul_f32_e32 v168, v168, v169
	v_mul_f32_e32 v148, v148, v130
	v_cvt_pk_bf16_f32 v148, v168, v148
	v_lshlrev_b32_e32 v168, 16, v149
	v_and_b32_e32 v149, 0xffff0000, v149
	v_lshlrev_b32_e32 v169, 16, v131
	v_and_b32_e32 v131, 0xffff0000, v131
	v_mul_f32_e32 v168, v168, v169
	v_mul_f32_e32 v149, v149, v131
	v_cvt_pk_bf16_f32 v149, v168, v149
	global_store_dwordx4 v[136:137], v[146:149], off
	v_add_co_u32_e32 v136, vcc, 0x30000, v136
	s_nop 1
	v_addc_co_u32_e32 v137, vcc, 0, v137, vcc
	s_waitcnt vmcnt(44) lgkmcnt(0)
	v_lshlrev_b32_e32 v168, 16, v150
	v_and_b32_e32 v150, 0xffff0000, v150
	v_lshlrev_b32_e32 v169, 16, v132
	v_and_b32_e32 v132, 0xffff0000, v132
	v_mul_f32_e32 v168, v168, v169
	v_mul_f32_e32 v150, v150, v132
	v_cvt_pk_bf16_f32 v150, v168, v150
	v_lshlrev_b32_e32 v168, 16, v151
	v_and_b32_e32 v151, 0xffff0000, v151
	v_lshlrev_b32_e32 v169, 16, v133
	v_and_b32_e32 v133, 0xffff0000, v133
	v_mul_f32_e32 v168, v168, v169
	v_mul_f32_e32 v151, v151, v133
	v_cvt_pk_bf16_f32 v151, v168, v151
	v_lshlrev_b32_e32 v168, 16, v152
	v_and_b32_e32 v152, 0xffff0000, v152
	v_lshlrev_b32_e32 v169, 16, v134
	v_and_b32_e32 v134, 0xffff0000, v134
	v_mul_f32_e32 v168, v168, v169
	v_mul_f32_e32 v152, v152, v134
	v_cvt_pk_bf16_f32 v152, v168, v152
	v_lshlrev_b32_e32 v168, 16, v153
	v_and_b32_e32 v153, 0xffff0000, v153
	v_lshlrev_b32_e32 v169, 16, v135
	v_and_b32_e32 v135, 0xffff0000, v135
	v_mul_f32_e32 v168, v168, v169
	v_mul_f32_e32 v153, v153, v135
	v_cvt_pk_bf16_f32 v153, v168, v153
	global_store_dwordx4 v[136:137], v[150:153], off
	s_branch .LBB0_1862
